# variant: one cached block per wave (half the cache traffic) with the branch-target touch
# speedup vs baseline: 1.0202x; 1.0005x over previous
_Z6k_iterILb0ELb0EEvPKfS1_PKiPK15HIP_vector_typeIfLj4EES7_S1_S1_S3_S1_PfS8_S1_S3_PDF16_PS5_SA_PiSA_SB_:
	s_and_b32 s38, s0, 0xfffff000
	s_mov_b32 s39, s1
	s_load_dwordx2 s[8:9], s[0:1], 0x80
	s_load_dwordx4 s[4:7], s[0:1], 0x70
	s_load_dwordx4 s[16:19], s[0:1], 0x40
	v_readfirstlane_b32 s12, v0
	v_cmp_gt_u32_e64 s[14:15], 64, v0
	v_lshlrev_b32_e32 v1, 2, v0
	s_and_saveexec_b64 s[10:11], s[14:15]
	v_mov_b32_e32 v2, 0
	ds_write_b32 v1, v2 offset:5152
	s_or_b64 exec, exec, s[10:11]
	s_lshl_b32 s3, s2, 5
	s_and_b32 s3, s3, 0xe0
	s_lshr_b32 s2, s2, 3
	s_add_i32 s2, s3, s2
	s_lshl_b32 s25, s2, 6
	v_and_b32_e32 v2, 31, v0
	v_or_b32_e32 v4, s25, v2
	v_mov_b32_e32 v5, 0
	s_lshr_b32 s27, s12, 6
	s_lshl_b32 s32, s27, 2
	s_lshr_b32 s32, 0x73261540, s32
	s_lshl_b32 s32, s32, 5
	s_and_b32 s32, s32, 0xe0
	v_or_b32_e32 v176, s32, v2
	v_lshlrev_b32_e32 v177, 4, v176
	v_add_u32_e32 v178, 0x1000, v177
	v_add_u32_e32 v179, 0x2000, v177
	v_add_u32_e32 v180, 0x3000, v177
	v_add_u32_e32 v181, 0x4000, v177
	v_add_u32_e32 v182, 0x5000, v177
	s_mov_b32 s3, 0
	s_lshl_b64 s[34:35], s[2:3], 16
	s_lshl_b32 s33, s2, 2
	s_waitcnt lgkmcnt(0)
	s_load_dword s24, s[8:9], s33 offset:0x0
	s_add_u32 s20, s4, s34
	s_addc_u32 s21, s5, s35
	v_lshl_add_u64 v[4:5], v[4:5], 4, s[6:7]
	global_load_dwordx3 v[30:32], v[4:5], off
	global_load_dwordx3 v[26:28], v[4:5], off offset:512
	global_load_dwordx4 v[2:5], v177, s[20:21]
	global_load_dwordx4 v[6:9], v178, s[20:21]
	global_load_dwordx4 v[10:13], v179, s[20:21]
	global_load_dwordx4 v[14:17], v180, s[20:21]
	global_load_dwordx4 v[18:21], v181, s[20:21]
	global_load_dwordx4 v[22:25], v182, s[20:21]
	s_cmp_eq_u32 s27, 0
	s_cbranch_scc1 .Lffc_touch_14
	s_cmp_eq_u32 s27, 1
	s_cbranch_scc1 .Lffc_touch_19
	s_cmp_eq_u32 s27, 2
	s_cbranch_scc1 .Lffc_touch_11
	s_cmp_eq_u32 s27, 3
	s_cbranch_scc1 .Lffc_touch_15
	s_cmp_eq_u32 s27, 4
	s_cbranch_scc1 .Lffc_touch_31
	s_cmp_eq_u32 s27, 5
	s_cbranch_scc1 .Lffc_touch_37
	s_cmp_eq_u32 s27, 6
	s_cbranch_scc1 .Lffc_touch_39

_Z6k_iterILb0ELb1EEvPKfS1_PKiPK15HIP_vector_typeIfLj4EES7_S1_S1_S3_S1_PfS8_S1_S3_PDF16_PS5_SA_PiSA_SB_:
	s_and_b32 s38, s0, 0xfffff000
	s_mov_b32 s39, s1
	s_load_dwordx2 s[8:9], s[0:1], 0x80
	s_load_dwordx4 s[4:7], s[0:1], 0x70
	s_load_dwordx4 s[16:19], s[0:1], 0x40
	s_load_dwordx2 s[22:23], s[0:1], 0x50
	s_load_dwordx2 s[42:43], s[0:1], 0x88
	v_readfirstlane_b32 s12, v0
	v_cmp_gt_u32_e64 s[14:15], 64, v0
	v_lshlrev_b32_e32 v1, 2, v0
	s_and_saveexec_b64 s[10:11], s[14:15]
	v_mov_b32_e32 v2, 0
	ds_write_b32 v1, v2 offset:5152
	s_or_b64 exec, exec, s[10:11]
	s_lshl_b32 s3, s2, 5
	s_and_b32 s3, s3, 0xe0
	s_lshr_b32 s2, s2, 3
	s_add_i32 s2, s3, s2
	s_lshl_b32 s29, s2, 6
	v_and_b32_e32 v2, 31, v0
	v_or_b32_e32 v4, s29, v2
	v_mov_b32_e32 v5, 0
	s_lshr_b32 s30, s12, 6
	s_lshl_b32 s32, s30, 2
	s_lshr_b32 s32, 0x73261540, s32
	s_lshl_b32 s32, s32, 5
	s_and_b32 s32, s32, 0xe0
	v_or_b32_e32 v176, s32, v2
	v_lshlrev_b32_e32 v177, 4, v176
	v_add_u32_e32 v178, 0x1000, v177
	v_add_u32_e32 v179, 0x2000, v177
	v_add_u32_e32 v180, 0x3000, v177
	v_add_u32_e32 v181, 0x4000, v177
	v_add_u32_e32 v182, 0x5000, v177
	s_mov_b32 s3, 0
	s_lshl_b64 s[34:35], s[2:3], 16
	s_lshl_b32 s33, s2, 2
	s_waitcnt lgkmcnt(0)
	s_load_dword s26, s[8:9], s33 offset:0x0
	s_add_u32 s20, s4, s34
	s_addc_u32 s21, s5, s35
	v_lshl_add_u64 v[4:5], v[4:5], 4, s[6:7]
	global_load_dwordx3 v[30:32], v[4:5], off
	global_load_dwordx3 v[26:28], v[4:5], off offset:512
	global_load_dwordx4 v[2:5], v177, s[20:21]
	global_load_dwordx4 v[6:9], v178, s[20:21]
	global_load_dwordx4 v[10:13], v179, s[20:21]
	global_load_dwordx4 v[14:17], v180, s[20:21]
	global_load_dwordx4 v[18:21], v181, s[20:21]
	global_load_dwordx4 v[22:25], v182, s[20:21]
	s_cmp_eq_u32 s30, 0
	s_cbranch_scc1 .Lftc_touch_14
	s_cmp_eq_u32 s30, 1
	s_cbranch_scc1 .Lftc_touch_19
	s_cmp_eq_u32 s30, 2
	s_cbranch_scc1 .Lftc_touch_11
	s_cmp_eq_u32 s30, 3
	s_cbranch_scc1 .Lftc_touch_15
	s_cmp_eq_u32 s30, 4
	s_cbranch_scc1 .Lftc_touch_31
	s_cmp_eq_u32 s30, 5
	s_cbranch_scc1 .Lftc_touch_37
	s_cmp_eq_u32 s30, 6
	s_cbranch_scc1 .Lftc_touch_39

.LBB4_39:
	s_waitcnt vmcnt(5)
	v_rcp_f32_e32 v2, v133
	s_waitcnt vmcnt(4)
	v_rcp_f32_e32 v3, v132
	s_waitcnt vmcnt(3)
	v_rcp_f32_e32 v4, v131
	v_cmp_lt_f32_e32 vcc, 0, v133
	s_waitcnt vmcnt(2)
	v_rcp_f32_e32 v5, v130
	s_waitcnt vmcnt(1)
	v_rcp_f32_e32 v6, v129
	v_cndmask_b32_e32 v2, 0, v2, vcc
	v_cmp_lt_f32_e32 vcc, 0, v132
	s_waitcnt vmcnt(0)
	v_rcp_f32_e32 v7, v128
	s_getpc_b64 s[36:37]
	s_sub_u32 s36, s36, 0x9638
	s_subb_u32 s37, s37, 0
	v_lshlrev_b32_e32 v183, 6, v0
	v_min_u32_e32 v183, 0x1d80, v183
	global_load_dword v183, v183, s[36:37]
	v_lshlrev_b32_e32 v182, 6, v38
	global_load_dword v182, v182, s[38:39]
	s_lshl_b32 s40, s29, 10
	s_add_u32 s40, s42, s40
	s_addc_u32 s41, s43, 0
	v_lshlrev_b32_e32 v181, 6, v0
	v_and_b32_e32 v181, 0x7fc0, v181
	global_load_dword v181, v181, s[40:41]
	s_mov_b32 s4, 0x42c80000
	v_cndmask_b32_e32 v3, 0, v3, vcc
	v_cmp_lt_f32_e32 vcc, 0, v131
	v_cmp_ngt_f32_e64 s[2:3], s4, v3
	s_mov_b64 s[6:7], 0
	v_cndmask_b32_e32 v4, 0, v4, vcc
	v_cmp_lt_f32_e32 vcc, 0, v130
	s_nop 1
	v_cndmask_b32_e32 v5, 0, v5, vcc
	v_cmp_lt_f32_e32 vcc, 0, v129
	s_nop 1
	v_cndmask_b32_e32 v6, 0, v6, vcc
	v_cmp_lt_f32_e32 vcc, 0, v128
	s_nop 1
	v_cndmask_b32_e32 v7, 0, v7, vcc
	v_cmp_ngt_f32_e32 vcc, s4, v2
	s_or_b64 s[2:3], vcc, s[2:3]
	v_cmp_ngt_f32_e32 vcc, s4, v4
	s_or_b64 s[2:3], s[2:3], vcc
	v_cmp_ngt_f32_e32 vcc, s4, v5
	s_or_b64 s[2:3], s[2:3], vcc
	v_cmp_ngt_f32_e32 vcc, s4, v6
	s_or_b64 s[2:3], s[2:3], vcc
	v_cmp_ngt_f32_e32 vcc, s4, v7
	s_or_b64 s[2:3], s[2:3], vcc
	v_cndmask_b32_e64 v8, 0, 1, s[2:3]
	v_cmp_ne_u32_e32 vcc, 0, v8
	s_cmp_eq_u64 vcc, 0
	s_cselect_b64 s[2:3], -1, 0
	v_cndmask_b32_e64 v8, 0, 1, s[2:3]
	s_nop 0
	v_readfirstlane_b32 s2, v8
	s_bitcmp0_b32 s2, 0
	s_cbranch_scc0 .LBB4_45
	s_cmp_lt_i32 s28, 4
	s_cbranch_scc1 .LBB4_46
	s_cmp_gt_i32 s28, 4
	s_cbranch_scc0 .LBB4_47
	s_mov_b64 s[4:5], -1
	v_mov_b32_e32 v8, 0
	s_cmp_gt_i32 s28, 5
	v_mov_b32_e32 v167, 0
	v_mov_b32_e32 v166, 0
	v_mov_b32_e32 v165, 0
	v_mov_b32_e32 v164, 0
	v_mov_b32_e32 v162, 0
	v_mov_b32_e32 v160, 0
	v_mov_b32_e32 v159, 0
	v_mov_b32_e32 v157, 0
	v_mov_b32_e32 v151, 0
	v_mov_b32_e32 v149, 0
	v_mov_b32_e32 v147, 0
	v_mov_b32_e32 v146, 0
	v_mov_b32_e32 v144, 0
	v_mov_b32_e32 v143, 0
	v_mov_b32_e32 v152, 0
	v_mov_b32_e32 v153, 0
	v_mov_b32_e32 v154, 0
	v_mov_b32_e32 v155, 0
	v_mov_b32_e32 v156, 0
	v_mov_b32_e32 v158, 0
	v_mov_b32_e32 v161, 0
	v_mov_b32_e32 v163, 0
	v_mov_b32_e32 v168, 0
	v_mov_b32_e32 v169, 0
	v_mov_b32_e32 v170, 0
	v_mov_b32_e32 v171, 0
	v_mov_b32_e32 v172, 0
	v_mov_b32_e32 v173, 0
	v_mov_b32_e32 v174, 0
	v_mov_b32_e32 v145, 0
	v_mov_b32_e32 v148, 0
	v_mov_b32_e32 v150, 0
	s_cbranch_scc0 .LBB4_50
	s_cmp_eq_u32 s28, 6
	s_cbranch_scc0 .LBB4_49
	v_mov_b32_e32 v145, 0
	v_mov_b32_e32 v148, 0
	v_mov_b32_e32 v150, 0
	v_mov_b32_e32 v143, 0
	v_mov_b32_e32 v144, 0
	v_mov_b32_e32 v146, 0
	v_mov_b32_e32 v147, 0
	v_mov_b32_e32 v149, 0
	v_mov_b32_e32 v151, 0
	v_mov_b32_e32 v152, 0
	v_mov_b32_e32 v153, 0
	v_mov_b32_e32 v154, 0
	v_mov_b32_e32 v155, 0
	v_mov_b32_e32 v156, 0
	v_mov_b32_e32 v158, 0
	v_mov_b32_e32 v161, 0
	v_mov_b32_e32 v163, 0
	v_mov_b32_e32 v157, 0
	v_mov_b32_e32 v159, 0
	v_mov_b32_e32 v160, 0
	v_mov_b32_e32 v162, 0
	v_mov_b32_e32 v164, 0
	v_mov_b32_e32 v165, 0
	v_mov_b32_e32 v166, 0
	v_mov_b32_e32 v167, 0
	v_mov_b32_e32 v168, 0
	v_mov_b32_e32 v169, 0
	v_mov_b32_e32 v170, 0
	v_mov_b32_e32 v171, 0
	v_mov_b32_e32 v172, 0
	v_mov_b32_e32 v173, 0
	v_mov_b32_e32 v174, 0
	v_fma_mix_f32 v148, v43, v7, v148 op_sel_hi:[1,0,0]
	v_fma_mix_f32 v150, v45, v7, v150 op_sel_hi:[1,0,0]
	v_fma_mix_f32 v143, v50, v7, v143 op_sel_hi:[1,0,0]
	v_fma_mix_f32 v144, v54, v7, v144 op_sel_hi:[1,0,0]
	v_fma_mix_f32 v146, v58, v7, v146 op_sel_hi:[1,0,0]
	v_fma_mix_f32 v147, v61, v7, v147 op_sel_hi:[1,0,0]
	v_fma_mix_f32 v149, v64, v7, v149 op_sel_hi:[1,0,0]
	v_fma_mix_f32 v151, v66, v7, v151 op_sel_hi:[1,0,0]
	v_fma_mix_f32 v152, v43, v7, v152 op_sel:[1,0,0] op_sel_hi:[1,0,0]
	v_fma_mix_f32 v153, v45, v7, v153 op_sel:[1,0,0] op_sel_hi:[1,0,0]
	v_fma_mix_f32 v154, v50, v7, v154 op_sel:[1,0,0] op_sel_hi:[1,0,0]
	v_fma_mix_f32 v155, v54, v7, v155 op_sel:[1,0,0] op_sel_hi:[1,0,0]
	v_fma_mix_f32 v156, v58, v7, v156 op_sel:[1,0,0] op_sel_hi:[1,0,0]
	v_fma_mix_f32 v158, v61, v7, v158 op_sel:[1,0,0] op_sel_hi:[1,0,0]
	v_fma_mix_f32 v161, v64, v7, v161 op_sel:[1,0,0] op_sel_hi:[1,0,0]
	v_fma_mix_f32 v163, v66, v7, v163 op_sel:[1,0,0] op_sel_hi:[1,0,0]
	v_fma_mix_f32 v157, v72, v7, v157 op_sel_hi:[1,0,0]
	v_fma_mix_f32 v159, v76, v7, v159 op_sel_hi:[1,0,0]
	v_fma_mix_f32 v160, v83, v7, v160 op_sel_hi:[1,0,0]
	v_fma_mix_f32 v162, v85, v7, v162 op_sel_hi:[1,0,0]
	v_fma_mix_f32 v164, v89, v7, v164 op_sel_hi:[1,0,0]
	v_fma_mix_f32 v165, v92, v7, v165 op_sel_hi:[1,0,0]
	v_fma_mix_f32 v166, v95, v7, v166 op_sel_hi:[1,0,0]
	v_fma_mix_f32 v167, v96, v7, v167 op_sel_hi:[1,0,0]
	v_fma_mix_f32 v168, v72, v7, v168 op_sel:[1,0,0] op_sel_hi:[1,0,0]
	v_fma_mix_f32 v169, v76, v7, v169 op_sel:[1,0,0] op_sel_hi:[1,0,0]
	v_fma_mix_f32 v170, v83, v7, v170 op_sel:[1,0,0] op_sel_hi:[1,0,0]
	v_fma_mix_f32 v171, v85, v7, v171 op_sel:[1,0,0] op_sel_hi:[1,0,0]
	v_fma_mix_f32 v172, v89, v7, v172 op_sel:[1,0,0] op_sel_hi:[1,0,0]
	v_fma_mix_f32 v173, v92, v7, v173 op_sel:[1,0,0] op_sel_hi:[1,0,0]
	v_fma_mix_f32 v174, v95, v7, v174 op_sel:[1,0,0] op_sel_hi:[1,0,0]
	v_fma_mix_f32 v145, v96, v7, v145 op_sel:[1,0,0] op_sel_hi:[1,0,0]
	s_branch .LBB4_50
